# pool mixer: token rows staged in LDS (12 coalesced loads per tile instead of a scattered load per window row), weight fragments loaded at the top of each K-step, operands swapped so the epilogue store
# speedup vs baseline: 1.0276x; 1.0118x over previous
; __device__ __forceinline__ void phase_p0(Frame& F, const Ptrs& P) {
;     ...
;         for (int r0 = gw * 4; r0 < 2 * NEXP; r0 += NGW * 4) {
;             const int ly = r0 >= NEXP, e0 = r0 - ly * NEXP; unsigned char* tab = tabT + (size_t)ly * 4 * NEXP * 128;
;             f32x4 a[4][4], g[4];
; #pragma unroll
;             for (int q = 0; q < 4; ++q)
; #pragma unroll
;                 for (int j = 0; j < 4; ++j) a[q][j] = *(const f32x4*)(srcT + (size_t)(r0 + q) * DM + 256 * j + 4 * lane);
; #pragma unroll
;             for (int j = 0; j < 4; ++j) { g[j] = (f32x4){scale, scale, scale, scale}; if (!tb) g[j] = g[j] * *(const f32x4*)(P.norm_ffn + (ly ? DM : 0) + 256 * j + 4 * lane); }
.LBB0_227:
	v_add_co_u32_e32 v2, vcc, 0xffffd000, v92
	s_cmpk_gt_i32 s25, 0x3fff
	s_nop 0
	v_addc_co_u32_e32 v3, vcc, -1, v93, vcc
	global_load_dwordx4 v[78:81], v[2:3], off offset:-3072
	global_load_dwordx4 v[74:77], v[2:3], off offset:-2048
	global_load_dwordx4 v[70:73], v[2:3], off offset:-1024
	global_load_dwordx4 v[66:69], v[2:3], off
	v_add_co_u32_e32 v2, vcc, 0xffffe000, v92
	s_cselect_b64 s[18:19], -1, 0
	s_nop 0
	v_addc_co_u32_e32 v3, vcc, -1, v93, vcc
	global_load_dwordx4 v[62:65], v[2:3], off offset:-3072
	global_load_dwordx4 v[58:61], v[2:3], off offset:-2048
	global_load_dwordx4 v[54:57], v[2:3], off offset:-1024
	global_load_dwordx4 v[50:53], v[2:3], off
	v_add_co_u32_e32 v2, vcc, 0xfffff000, v92
	s_and_b64 s[6:7], s[18:19], exec
	s_nop 0
	v_addc_co_u32_e32 v3, vcc, -1, v93, vcc
	global_load_dwordx4 v[46:49], v[2:3], off offset:-3072
	global_load_dwordx4 v[42:45], v[2:3], off offset:-2048
	global_load_dwordx4 v[38:41], v[2:3], off offset:-1024
	global_load_dwordx4 v[34:37], v[92:93], off offset:-4096
	global_load_dwordx4 v[26:29], v[92:93], off offset:-3072
	global_load_dwordx4 v[14:17], v[92:93], off offset:-2048
	global_load_dwordx4 v[6:9], v[92:93], off offset:-1024
	s_nop 0
	global_load_dwordx4 v[2:5], v[92:93], off
	s_cselect_b32 s8, 0x1000, 0
	v_lshl_add_u64 v[94:95], v[84:85], 0, s[8:9]
	s_and_b64 vcc, exec, s[4:5]
	s_cbranch_vccnz .Lp0g_skip
	global_load_dwordx4 v[152:155], v[94:95], off
	global_load_dwordx4 v[156:159], v[94:95], off offset:1024
	global_load_dwordx4 v[160:163], v[94:95], off offset:2048
	global_load_dwordx4 v[164:167], v[94:95], off offset:3072
.Lp0g_skip:
	s_and_b64 vcc, exec, s[4:5]
	s_waitcnt vmcnt(0)
	v_mov_b64_e32 v[32:33], v[2:3]
	v_mov_b64_e32 v[30:31], v[0:1]
	v_mov_b32_e32 v31, v0
	v_mov_b32_e32 v32, v0
	v_mov_b32_e32 v33, v0
	s_cbranch_vccnz .LBB0_229
	v_mov_b32_e32 v1, v0
	v_pk_mul_f32 v[32:33], v[0:1], v[154:155]
	v_pk_mul_f32 v[30:31], v[88:89], v[152:153]
.LBB0_229:
	v_mov_b64_e32 v[24:25], v[2:3]
	v_mov_b64_e32 v[22:23], v[0:1]
	s_and_b64 vcc, exec, s[4:5]
	v_mov_b32_e32 v23, v0
	v_mov_b32_e32 v24, v0
	v_mov_b32_e32 v25, v0
	s_cbranch_vccnz .LBB0_231
	v_mov_b32_e32 v1, v0
	v_pk_mul_f32 v[24:25], v[0:1], v[158:159]
	v_pk_mul_f32 v[22:23], v[88:89], v[156:157]
.LBB0_231:
	v_mov_b64_e32 v[20:21], v[2:3]
	v_mov_b64_e32 v[18:19], v[0:1]
	s_and_b64 vcc, exec, s[4:5]
	v_mov_b32_e32 v19, v0
	v_mov_b32_e32 v20, v0
	v_mov_b32_e32 v21, v0
	s_cbranch_vccnz .LBB0_233
	v_mov_b32_e32 v1, v0
	v_pk_mul_f32 v[20:21], v[0:1], v[162:163]
	v_pk_mul_f32 v[18:19], v[88:89], v[160:161]
.LBB0_233:
	v_mov_b64_e32 v[12:13], v[2:3]
	v_mov_b64_e32 v[10:11], v[0:1]
	s_and_b64 vcc, exec, s[4:5]
	v_mov_b32_e32 v11, v0
	v_mov_b32_e32 v12, v0
	v_mov_b32_e32 v13, v0
	s_cbranch_vccnz .LBB0_235
	v_mov_b32_e32 v1, v0
	v_pk_mul_f32 v[12:13], v[0:1], v[166:167]
	v_pk_mul_f32 v[10:11], v[88:89], v[164:165]

; __device__ __forceinline__ unsigned pk2(float lo, float hi) { const f32x2_pk v = {lo, hi}; return __builtin_bit_cast(unsigned, __builtin_convertvector(v, bf16x2)); }
; __device__ __forceinline__ float lsn2q(float z2) { return -(fmaxf(z2, 0.f) + __builtin_amdgcn_logf(1.f + __builtin_amdgcn_exp2f(-fabsf(z2)))); }
; template <int KIND, int MODE> ...
;     ...
;         float l2[16]; float sLo = 0.f, sHi = 0.f;
; #pragma unroll
;         for (int r = 0; r < 16; ++r) l2[r] = lsn2q(S[r]);
; #pragma unroll
;         for (int r = 0; r < 8; ++r) { sLo += l2[r]; sHi += l2[8 + r]; }
;         const float pLo = __shfl_xor(sLo, 32), pHi = __shfl_xor(sHi, 32);
;         float run = hi ? R : R + pHi;
; #pragma unroll
;         for (int r = 15; r >= 8; --r) { p[r] = __builtin_amdgcn_exp2f(S[r] + l2[r] + run); run += l2[r]; }
;         run = hi ? (R + sHi + pHi) : (R + pHi + sHi + pLo);
; #pragma unroll
;         for (int r = 7; r >= 0; --r) { p[r] = __builtin_amdgcn_exp2f(S[r] + l2[r] + run); run += l2[r]; }
;         R += (sLo + sHi) + (pLo + pHi);
;     }
;     u32x4 w0, w1;
;     w0.x = pk2(p[0], p[1]); w0.y = pk2(p[2], p[3]); w0.z = pk2(p[4], p[5]); w0.w = pk2(p[6], p[7]);
;     w1.x = pk2(p[8], p[9]); w1.y = pk2(p[10], p[11]); w1.z = pk2(p[12], p[13]); w1.w = pk2(p[14], p[15]);
;     const bf16x8 pf0 = __builtin_bit_cast(bf16x8, w0), pf1 = __builtin_bit_cast(bf16x8, w1);
;     O0 = __builtin_amdgcn_mfma_f32_32x32x16_bf16(vf[0][0], pf0, O0, 0, 0, 0); O0 = __builtin_amdgcn_mfma_f32_32x32x16_bf16(vf[1][0], pf1, O0, 0, 0, 0);
;     O1 = __builtin_amdgcn_mfma_f32_32x32x16_bf16(vf[0][1], pf0, O1, 0, 0, 0); O1 = __builtin_amdgcn_mfma_f32_32x32x16_bf16(vf[1][1], pf1, O1, 0, 0, 0);
.LBB0_583:
	s_cmp_lg_u32 s30, 0
	s_cbranch_scc0 .LBB0_588
	s_waitcnt vmcnt(7)
	v_mfma_f32_32x32x16_bf16 v[32:47], v[124:127], v[76:79], 0
	v_and_b32_e32 v148, 64, v139
	v_add_u32_e32 v148, 64, v148
	s_waitcnt vmcnt(6)
	v_mfma_f32_32x32x16_bf16 v[32:47], v[120:123], v[72:75], v[32:47]
	s_waitcnt vmcnt(5)
	v_mfma_f32_32x32x16_bf16 v[32:47], v[116:119], v[68:71], v[32:47]
	s_waitcnt vmcnt(4)
	v_mfma_f32_32x32x16_bf16 v[32:47], v[112:115], v[64:67], v[32:47]
	s_nop 11
	v_exp_f32_e64 v56, -|v34|
	v_exp_f32_e64 v57, -|v35|
	v_exp_f32_e64 v58, -|v36|
	v_exp_f32_e64 v59, -|v37|
	v_add_f32_e32 v56, 1.0, v56
	v_add_f32_e32 v57, 1.0, v57
	v_exp_f32_e64 v54, -|v32|
	v_exp_f32_e64 v55, -|v33|
	v_add_f32_e32 v58, 1.0, v58
	v_add_f32_e32 v59, 1.0, v59
	v_log_f32_e32 v56, v56
	v_log_f32_e32 v57, v57
	v_log_f32_e32 v58, v58
	v_log_f32_e32 v59, v59
	v_max_f32_e32 v50, 0, v34
	v_max_f32_e32 v51, 0, v35
	v_max_f32_e32 v52, 0, v36
	v_max_f32_e32 v53, 0, v37
	v_add_f32_e32 v54, 1.0, v54
	v_add_f32_e32 v55, 1.0, v55
	v_pk_add_f32 v[50:51], v[50:51], v[56:57]
	v_exp_f32_e64 v57, -|v40|
	v_exp_f32_e64 v60, -|v38|
	v_exp_f32_e64 v61, -|v39|
	v_log_f32_e32 v54, v54
	v_log_f32_e32 v55, v55
	v_pk_add_f32 v[52:53], v[52:53], v[58:59]
	v_exp_f32_e64 v59, -|v41|
	v_max_f32_e32 v48, 0, v32
	v_max_f32_e32 v49, 0, v33
	v_add_f32_e32 v57, 1.0, v57
	v_add_f32_e32 v60, 1.0, v60
	v_pk_add_f32 v[48:49], v[48:49], v[54:55]
	v_add_f32_e32 v54, 1.0, v61
	v_log_f32_e32 v58, v57
	v_add_f32_e32 v57, 1.0, v59
	v_log_f32_e32 v60, v60
	v_log_f32_e32 v61, v54
	v_log_f32_e32 v59, v57
	v_max_f32_e32 v62, v38, v38
	v_max_f32_e32 v54, 0, v62
	v_max_f32_e32 v55, 0, v39
	v_max_f32_e32 v56, 0, v40
	v_max_f32_e32 v57, 0, v41
	v_pk_add_f32 v[54:55], v[54:55], v[60:61]
	v_exp_f32_e64 v60, -|v42|
	v_pk_add_f32 v[56:57], v[56:57], v[58:59]
	v_exp_f32_e64 v59, -|v43|
	v_max_f32_e32 v61, v42, v42
	v_add_f32_e32 v58, 1.0, v60
	v_log_f32_e32 v58, v58
	v_add_f32_e32 v59, 1.0, v59
	v_log_f32_e32 v59, v59
	v_max_f32_e32 v60, 0, v61
	v_max_f32_e32 v61, 0, v43
	v_pk_add_f32 v[58:59], v[60:61], v[58:59]
	v_exp_f32_e64 v61, -|v44|
	v_exp_f32_e64 v63, -|v45|
	v_max_f32_e32 v60, 0, v44
	v_add_f32_e32 v61, 1.0, v61
	v_log_f32_e32 v62, v61
	v_add_f32_e32 v61, 1.0, v63
	v_log_f32_e32 v63, v61
	v_max_f32_e32 v61, 0, v45
	v_exp_f32_e64 v146, -|v46|
	v_pk_add_f32 v[60:61], v[60:61], v[62:63]
	v_exp_f32_e64 v63, -|v47|
	v_max_f32_e32 v147, v46, v46
	v_add_f32_e32 v62, 1.0, v146
	v_log_f32_e32 v62, v62
	v_add_f32_e32 v63, 1.0, v63
	v_log_f32_e32 v63, v63
	v_max_f32_e32 v146, 0, v147
	v_max_f32_e32 v147, 0, v47
	v_pk_add_f32 v[62:63], v[146:147], v[62:63]
	v_sub_f32_e64 v147, -v56, v57
	v_sub_f32_e32 v147, v147, v58
	v_sub_f32_e32 v147, v147, v59
	v_sub_f32_e32 v147, v147, v60
	v_sub_f32_e32 v147, v147, v61
	v_sub_f32_e32 v147, v147, v62
	v_sub_f32_e32 v155, v147, v63
	v_xor_b32_e32 v147, 32, v139
	v_cmp_lt_i32_e32 vcc, v147, v148
	v_sub_f32_e64 v146, -v48, v49
	v_sub_f32_e32 v146, v146, v50
	v_cndmask_b32_e32 v147, v139, v147, vcc
	v_lshlrev_b32_e32 v147, 2, v147
	ds_bpermute_b32 v156, v147, v155
	v_sub_f32_e32 v146, v146, v51
	v_sub_f32_e32 v146, v146, v52
	v_sub_f32_e32 v146, v146, v53
	v_sub_f32_e32 v146, v146, v54
	v_sub_f32_e32 v157, v146, v55
	s_waitcnt lgkmcnt(0)
	v_add_f32_e32 v146, v144, v156
	ds_bpermute_b32 v154, v147, v157
	v_cndmask_b32_e64 v147, v144, v146, s[2:3]
	v_sub_f32_e32 v47, v47, v63
	v_add_f32_e32 v47, v147, v47
	v_exp_f32_e32 v153, v47
	v_mov_b32_e32 v47, v147
	v_pk_add_f32 v[46:47], v[46:47], v[62:63] neg_lo:[0,1] neg_hi:[0,1]
	v_pk_mov_b32 v[62:63], v[60:61], v[62:63] op_sel:[1,0]
	v_add_f32_e32 v150, v47, v46
	v_mov_b32_e32 v46, v45
	v_pk_add_f32 v[46:47], v[46:47], v[62:63] neg_lo:[0,1] neg_hi:[0,1]
	v_sub_f32_e32 v39, v39, v55
	v_add_f32_e32 v45, v46, v47
	v_exp_f32_e32 v62, v45
	v_mov_b32_e32 v45, v47
	v_pk_add_f32 v[44:45], v[44:45], v[60:61] neg_lo:[0,1] neg_hi:[0,1]
	v_pk_mov_b32 v[46:47], v[58:59], v[60:61] op_sel:[1,0]
	v_add_f32_e32 v63, v44, v45
	v_mov_b32_e32 v44, v43
	v_pk_add_f32 v[44:45], v[44:45], v[46:47] neg_lo:[0,1] neg_hi:[0,1]
	s_nop 0
	v_add_f32_e32 v43, v44, v45
	v_exp_f32_e32 v60, v43
	v_mov_b32_e32 v43, v45
	v_pk_add_f32 v[42:43], v[42:43], v[58:59] neg_lo:[0,1] neg_hi:[0,1]
	v_pk_mov_b32 v[44:45], v[56:57], v[58:59] op_sel:[1,0]
	v_add_f32_e32 v61, v42, v43
	v_mov_b32_e32 v42, v41
	v_pk_add_f32 v[42:43], v[42:43], v[44:45] neg_lo:[0,1] neg_hi:[0,1]
	s_nop 0
	v_add_f32_e32 v41, v42, v43
	v_exp_f32_e32 v58, v41
	v_mov_b32_e32 v41, v43
	v_pk_add_f32 v[40:41], v[40:41], v[56:57] neg_lo:[0,1] neg_hi:[0,1]
	s_nop 0
	v_add_f32_e32 v40, v40, v41
	v_exp_f32_e32 v56, v40
	v_add_f32_e32 v40, v144, v155
	v_add_f32_e32 v41, v146, v155
	v_add_f32_e32 v40, v40, v156
	s_waitcnt lgkmcnt(0)
	v_add_f32_e32 v41, v41, v154
	v_cndmask_b32_e64 v40, v40, v41, s[2:3]
	v_add_f32_e32 v39, v39, v40
	v_exp_f32_e32 v42, v39
	v_mov_b32_e32 v39, v40
	v_pk_add_f32 v[38:39], v[38:39], v[54:55] neg_lo:[0,1] neg_hi:[0,1]
	v_pk_mov_b32 v[40:41], v[52:53], v[54:55] op_sel:[1,0]
	v_add_f32_e32 v43, v38, v39
	v_mov_b32_e32 v38, v37
	v_pk_add_f32 v[38:39], v[38:39], v[40:41] neg_lo:[0,1] neg_hi:[0,1]
	s_nop 0
	v_add_f32_e32 v37, v38, v39
	v_exp_f32_e32 v40, v37
	v_mov_b32_e32 v37, v39
	v_pk_add_f32 v[36:37], v[36:37], v[52:53] neg_lo:[0,1] neg_hi:[0,1]
	v_pk_mov_b32 v[38:39], v[50:51], v[52:53] op_sel:[1,0]
	v_add_f32_e32 v41, v36, v37
	v_mov_b32_e32 v36, v35
	v_pk_add_f32 v[36:37], v[36:37], v[38:39] neg_lo:[0,1] neg_hi:[0,1]
	s_nop 0
	v_add_f32_e32 v35, v36, v37
	v_exp_f32_e32 v38, v35
	v_mov_b32_e32 v35, v37
	v_pk_add_f32 v[34:35], v[34:35], v[50:51] neg_lo:[0,1] neg_hi:[0,1]
	v_pk_mov_b32 v[36:37], v[48:49], v[50:51] op_sel:[1,0]
	v_add_f32_e32 v39, v34, v35
	v_mov_b32_e32 v34, v33
	v_pk_add_f32 v[34:35], v[34:35], v[36:37] neg_lo:[0,1] neg_hi:[0,1]
	v_exp_f32_e32 v36, v43
	v_add_f32_e32 v33, v34, v35
	v_exp_f32_e32 v34, v33
	v_mov_b32_e32 v33, v35
	v_pk_add_f32 v[32:33], v[32:33], v[48:49] neg_lo:[0,1] neg_hi:[0,1]
	v_exp_f32_e32 v35, v41
	v_add_f32_e32 v32, v32, v33
	v_exp_f32_e32 v32, v32
	v_exp_f32_e32 v33, v39
	v_exp_f32_e32 v48, v61
	v_exp_f32_e32 v49, v63
	v_exp_f32_e32 v50, v150
	v_cvt_pk_bf16_f32 v146, v32, v34
	v_cvt_pk_bf16_f32 v147, v33, v38
	v_cvt_pk_bf16_f32 v148, v35, v40
	v_cvt_pk_bf16_f32 v149, v36, v42
	v_cvt_pk_bf16_f32 v150, v56, v58
	v_cvt_pk_bf16_f32 v151, v48, v60
	s_waitcnt vmcnt(3)
	v_mfma_f32_32x32x16_bf16 v[0:15], v[108:111], v[146:149], v[0:15]
	v_cvt_pk_bf16_f32 v152, v49, v62
	v_cvt_pk_bf16_f32 v153, v50, v153
	s_waitcnt vmcnt(1)
	v_mfma_f32_32x32x16_bf16 v[16:31], v[100:103], v[146:149], v[16:31]
	v_add_f32_e64 v146, v154, v156
	v_add_f32_e64 v147, v155, v157
	v_add_f32_e32 v146, v146, v147
	v_mfma_f32_32x32x16_bf16 v[0:15], v[104:107], v[150:153], v[0:15]
	s_waitcnt vmcnt(0)
	v_mfma_f32_32x32x16_bf16 v[16:31], v[96:99], v[150:153], v[16:31]
	s_cbranch_execnz .LBB0_586

; template <int KIND>
; __device__ __forceinline__ void attn_wave(const bf16_t* Qh, const bf16_t* Kh, const bf16_t* Vth, const int q0, const int lane, const float* CFh, const float slope2, const float* KMh, bf16_t* AOp) {
;     ...
;             attn_load_v(vf, Vth, kv0, r32, hi); const f32x16 bias = f32x16{};
;             if (it > 0) attn_load_k(kfn, Kh, kv0 - 32, r32p, hi);
;             if (it == nt - 1) attn_tile<1, 1>(qr, kf, vf, O0, O1, m, l, R, bias, kv0, q, hi, true); else attn_tile<1, 0>(qr, kf, vf, O0, O1, m, l, R, bias, kv0, q, hi, true);
; #pragma unroll
;             for (int d0 = 0; d0 < 4; ++d0) kf[d0] = kfn[d0];
;             if (__all(R < -200.f)) break; }
.LBB0_586:
	v_add_f32_e32 v144, v144, v146
	v_cmp_gt_f32_e32 vcc, s26, v144
	s_cmp_lg_u64 vcc, exec
	s_cselect_b64 s[0:1], -1, 0
	v_cmp_lt_i32_e32 vcc, 0, v145
	s_and_b64 s[0:1], vcc, s[0:1]
	s_sub_i32 s30, s30, 32
	s_and_b64 vcc, exec, s[0:1]
	s_cbranch_vccz .Lsb_exit
	s_waitcnt vmcnt(0)
	v_mov_b64_e32 v[114:115], v[82:83]
	v_mov_b32_e32 v145, v137
	v_mov_b64_e32 v[112:113], v[80:81]
	v_mov_b32_e32 v124, v92
	v_mov_b32_e32 v125, v93
	v_mov_b32_e32 v126, v94
	v_mov_b32_e32 v127, v95
	v_mov_b32_e32 v120, v88
	v_mov_b32_e32 v121, v89
	v_mov_b32_e32 v122, v90
	v_mov_b32_e32 v123, v91
	v_mov_b32_e32 v116, v84
	v_mov_b32_e32 v117, v85
	v_mov_b32_e32 v118, v86
	v_mov_b32_e32 v119, v87
	s_branch .LBB0_581
.Lsb_exit:
	s_nop 7
	v_mov_b64_e32 v[32:33], v[0:1]
	v_mov_b64_e32 v[34:35], v[2:3]
	v_mov_b64_e32 v[36:37], v[4:5]
	v_mov_b64_e32 v[38:39], v[6:7]
	v_mov_b64_e32 v[40:41], v[8:9]
	v_mov_b64_e32 v[42:43], v[10:11]
	v_mov_b64_e32 v[44:45], v[12:13]
	v_mov_b64_e32 v[46:47], v[14:15]
	v_mov_b64_e32 v[48:49], v[16:17]
	v_mov_b64_e32 v[50:51], v[18:19]
	v_mov_b64_e32 v[52:53], v[20:21]
	v_mov_b64_e32 v[54:55], v[22:23]
	v_mov_b64_e32 v[56:57], v[24:25]
	v_mov_b64_e32 v[58:59], v[26:27]
	v_mov_b64_e32 v[60:61], v[28:29]
	v_mov_b64_e32 v[62:63], v[30:31]
	s_branch .LBB0_572

; __device__ __forceinline__ int opaque_i(int v) { asm volatile("" : "+v"(v)); return v; }
; __device__ __forceinline__ void phase_pool(Frame& F, const bf16_t* XC, const bf16_t* PWT, const float* pool_scale, bf16_t* AO) {
;     const int gw = F.vcu * NWAVES + F.wave, NGW = F.G * NWAVES, lane = opaque_i(F.lane), r32 = lane & 31, hi = lane >> 5;
;     for (int it = gw; it < (TOK / 32) * 4; it += NGW) {
;         const int rnd = it / NGW, gq = it - rnd * NGW;
;         const int g = (rnd & 1) ? 3 - (gq & 3) : (gq & 3), t0 = (rnd * (NGW >> 2) + (gq >> 2)) * 32, t = t0 + r32, tl = t & 2047, w = 2 << g;
;         const int cnt = (tl + 1) < w ? (tl + 1) : w; const float rc = 1.f / (float)cnt;
;         f32x16 acc[4];
; #pragma unroll
;         for (int nb = 0; nb < 4; ++nb) acc[nb] = f32x16{};
; #pragma unroll 1
;         for (int kk = 0; kk < 8; ++kk) {
;             const int c0 = g * 128 + kk * 16 + hi * 8;
;             const u32x4 self = *(const u32x4*)(XC + (size_t)t * 512 + c0);
;             float s[8] = {0.f, 0.f, 0.f, 0.f, 0.f, 0.f, 0.f, 0.f};
;             for (int i = 0; i < cnt; ++i) { const u32x4 x = *(const u32x4*)(XC + (size_t)(t - i) * 512 + c0);
.LBB0_1343:
	s_abs_i32 s4, s6
	s_mul_hi_u32 s5, s4, s13
	s_mul_i32 s19, s5, s9
	s_ashr_i32 s0, s6, 31
	s_sub_i32 s4, s4, s19
	s_xor_b32 s0, s0, s12
	s_add_i32 s19, s5, 1
	s_sub_i32 s20, s4, s9
	s_cmp_ge_u32 s4, s9
	s_cselect_b32 s5, s19, s5
	s_cselect_b32 s4, s20, s4
	s_add_i32 s19, s5, 1
	s_cmp_ge_u32 s4, s9
	s_cselect_b32 s4, s19, s5
	s_xor_b32 s4, s4, s0
	s_sub_i32 s0, s4, s0
	s_mul_i32 s4, s0, s7
	s_sub_i32 s4, s6, s4
	s_bitcmp0_b32 s0, 0
	s_cselect_b32 s21, s10, s11
	s_mul_i32 s5, s8, s0
	s_ashr_i32 s22, s4, 2
	s_add_i32 s4, s22, s5
	s_lshl_b32 s19, s4, 5
	v_bitop3_b32 v0, s19, v96, v94 bitop3:0xc8
	s_lshl_b32 s23, 2, s21
	v_add_u32_e32 v0, 1, v0
	v_min_u32_e32 v0, s23, v0
	v_cvt_f32_ubyte0_e32 v1, v0
	v_div_scale_f32 v2, s[4:5], v1, v1, 1.0
	v_rcp_f32_e32 v3, v2
	v_or_b32_e32 v0, s19, v94
	s_mul_i32 s0, s14, s0
	s_lshl_b32 s4, s22, 5
	v_fma_f32 v4, -v2, v3, 1.0
	v_fmac_f32_e32 v3, v4, v3
	v_div_scale_f32 v4, vcc, 1.0, v1, 1.0
	v_mul_f32_e32 v5, v4, v3
	v_fma_f32 v6, -v2, v5, v4
	v_fmac_f32_e32 v5, v6, v3
	v_fma_f32 v2, -v2, v5, v4
	v_div_fmas_f32 v2, v2, v3, v5
	v_div_fixup_f32 v74, v2, v1, 1.0
	v_ashrrev_i32_e32 v1, 31, v0
	v_lshlrev_b64 v[0:1], 10, v[0:1]
	v_lshl_add_u64 v[78:79], s[96:97], 0, v[0:1]
	v_add_u16_e32 v0, s0, v94
	v_add_u16_e32 v0, s4, v0
	v_and_b32_e32 v0, 0x7ff, v0
	v_add_u32_e32 v0, 1, v0
	v_lshl_or_b32 v72, s21, 15, v95
	v_min_u32_e32 v0, s23, v0
	s_add_i32 s4, s4, s0
	s_lshl_b32 s20, s21, 7
	v_lshl_add_u64 v[80:81], v[70:71], 0, v[72:73]
	v_sub_u32_e32 v72, 0, v0
	v_add_u32_e32 v0, s4, v94
	v_add_u32_e32 v76, s20, v68
	v_ashrrev_i32_e32 v1, 31, v0
	v_lshlrev_b64 v[0:1], 10, v[0:1]
	v_ashrrev_i32_e32 v77, 31, v76
	v_lshl_add_u64 v[0:1], v[76:77], 1, v[0:1]
	v_mov_b32_e32 v75, v74
	v_lshl_add_u64 v[82:83], s[96:97], 0, v[0:1]
	s_mov_b32 s21, s1
	v_mov_b32_e32 v0, 0
	v_mov_b32_e32 v1, v73
	v_mov_b32_e32 v2, v73
	v_mov_b32_e32 v3, v73
	v_mov_b32_e32 v4, v73
	v_mov_b32_e32 v5, v73
	v_mov_b32_e32 v6, v73
	v_mov_b32_e32 v7, v73
	v_mov_b32_e32 v8, v73
	v_mov_b32_e32 v9, v73
	v_mov_b32_e32 v10, v73
	v_mov_b32_e32 v11, v73
	v_mov_b32_e32 v12, v73
	v_mov_b32_e32 v13, v73
	v_mov_b32_e32 v14, v73
	v_mov_b32_e32 v15, v73
	v_mov_b32_e32 v16, 0
	v_mov_b32_e32 v17, v73
	v_mov_b32_e32 v18, v73
	v_mov_b32_e32 v19, v73
	v_mov_b32_e32 v20, v73
	v_mov_b32_e32 v21, v73
	v_mov_b32_e32 v22, v73
	v_mov_b32_e32 v23, v73
	v_mov_b32_e32 v24, v73
	v_mov_b32_e32 v25, v73
	v_mov_b32_e32 v26, v73
	v_mov_b32_e32 v27, v73
	v_mov_b32_e32 v28, v73
	v_mov_b32_e32 v29, v73
	v_mov_b32_e32 v30, v73
	v_mov_b32_e32 v31, v73
	v_mov_b32_e32 v32, 0
	v_mov_b32_e32 v33, v73
	v_mov_b32_e32 v34, v73
	v_mov_b32_e32 v35, v73
	v_mov_b32_e32 v36, v73
	v_mov_b32_e32 v37, v73
	v_mov_b32_e32 v38, v73
	v_mov_b32_e32 v39, v73
	v_mov_b32_e32 v40, v73
	v_mov_b32_e32 v41, v73
	v_mov_b32_e32 v42, v73
	v_mov_b32_e32 v43, v73
	v_mov_b32_e32 v44, v73
	v_mov_b32_e32 v45, v73
	v_mov_b32_e32 v46, v73
	v_mov_b32_e32 v47, v73
	v_mov_b32_e32 v48, 0
	v_mov_b32_e32 v49, v73
	v_mov_b32_e32 v50, v73
	v_mov_b32_e32 v51, v73
	v_mov_b32_e32 v52, v73
	v_mov_b32_e32 v53, v73
	v_mov_b32_e32 v54, v73
	v_mov_b32_e32 v55, v73
	v_mov_b32_e32 v56, v73
	v_mov_b32_e32 v57, v73
	v_mov_b32_e32 v58, v73
	v_mov_b32_e32 v59, v73
	v_mov_b32_e32 v60, v73
	v_mov_b32_e32 v61, v73
	v_mov_b32_e32 v62, v73
	v_mov_b32_e32 v63, v73
	v_lshrrev_b32_e32 v150, 4, v208
	v_and_b32_e32 v151, 15, v208
	v_mul_u32_u24_e32 v148, 0x110, v150
	v_lshl_add_u32 v148, v151, 4, v148
	s_lshl_b32 s0, s74, 14
	v_add_u32_e32 v148, s0, v148
	v_add_u32_e32 v149, 15, v94
	v_mul_u32_u24_e32 v149, 0x110, v149
	v_lshl_add_u32 v149, v69, 2, v149
	v_add_u32_e32 v149, s0, v149
	v_add_u32_e32 v152, s19, v150
	v_subrev_u32_e32 v152, 15, v152
	s_lshl_b32 s4, s20, 1
	v_lshl_add_u32 v153, v151, 4, s4
	v_add_u32_e32 v154, 0, v152
	v_max_i32_e32 v154, 0, v154
	v_min_i32_e32 v154, 0x7fff, v154
	v_lshl_add_u32 v154, v154, 10, v153
	global_load_dwordx4 v[100:103], v154, s[96:97]
	v_add_u32_e32 v154, 4, v152
	v_max_i32_e32 v154, 0, v154
	v_min_i32_e32 v154, 0x7fff, v154
	v_lshl_add_u32 v154, v154, 10, v153
	global_load_dwordx4 v[104:107], v154, s[96:97]
	v_add_u32_e32 v154, 8, v152
	v_max_i32_e32 v154, 0, v154
	v_min_i32_e32 v154, 0x7fff, v154
	v_lshl_add_u32 v154, v154, 10, v153
	global_load_dwordx4 v[108:111], v154, s[96:97]
	v_add_u32_e32 v154, 12, v152
	v_max_i32_e32 v154, 0, v154
	v_min_i32_e32 v154, 0x7fff, v154
	v_lshl_add_u32 v154, v154, 10, v153
	global_load_dwordx4 v[112:115], v154, s[96:97]
	v_add_u32_e32 v154, 16, v152
	v_max_i32_e32 v154, 0, v154
	v_min_i32_e32 v154, 0x7fff, v154
	v_lshl_add_u32 v154, v154, 10, v153
	global_load_dwordx4 v[116:119], v154, s[96:97]
	v_add_u32_e32 v154, 20, v152
	v_max_i32_e32 v154, 0, v154
	v_min_i32_e32 v154, 0x7fff, v154
	v_lshl_add_u32 v154, v154, 10, v153
	global_load_dwordx4 v[120:123], v154, s[96:97]
	v_add_u32_e32 v154, 24, v152
	v_max_i32_e32 v154, 0, v154
	v_min_i32_e32 v154, 0x7fff, v154
	v_lshl_add_u32 v154, v154, 10, v153
	global_load_dwordx4 v[124:127], v154, s[96:97]
	v_add_u32_e32 v154, 28, v152
	v_max_i32_e32 v154, 0, v154
	v_min_i32_e32 v154, 0x7fff, v154
	v_lshl_add_u32 v154, v154, 10, v153
	global_load_dwordx4 v[128:131], v154, s[96:97]
	v_add_u32_e32 v154, 32, v152
	v_max_i32_e32 v154, 0, v154
	v_min_i32_e32 v154, 0x7fff, v154
	v_lshl_add_u32 v154, v154, 10, v153
	global_load_dwordx4 v[132:135], v154, s[96:97]
	v_add_u32_e32 v154, 36, v152
	v_max_i32_e32 v154, 0, v154
	v_min_i32_e32 v154, 0x7fff, v154
	v_lshl_add_u32 v154, v154, 10, v153
	global_load_dwordx4 v[136:139], v154, s[96:97]
	v_add_u32_e32 v154, 40, v152
	v_max_i32_e32 v154, 0, v154
	v_min_i32_e32 v154, 0x7fff, v154
	v_lshl_add_u32 v154, v154, 10, v153
	global_load_dwordx4 v[140:143], v154, s[96:97]
	v_add_u32_e32 v154, 44, v152
	v_max_i32_e32 v154, 0, v154
	v_min_i32_e32 v154, 0x7fff, v154
	v_lshl_add_u32 v154, v154, 10, v153
	global_load_dwordx4 v[144:147], v154, s[96:97]
	s_waitcnt vmcnt(0)
	ds_write_b128 v148, v[100:103]
	ds_write_b128 v148, v[104:107] offset:1088
	ds_write_b128 v148, v[108:111] offset:2176
	ds_write_b128 v148, v[112:115] offset:3264
	ds_write_b128 v148, v[116:119] offset:4352
	ds_write_b128 v148, v[120:123] offset:5440
	ds_write_b128 v148, v[124:127] offset:6528
	ds_write_b128 v148, v[128:131] offset:7616
	ds_write_b128 v148, v[132:135] offset:8704
	ds_write_b128 v148, v[136:139] offset:9792
	ds_write_b128 v148, v[140:143] offset:10880
	ds_write_b128 v148, v[144:147] offset:11968
	s_waitcnt lgkmcnt(0)
; __device__ __forceinline__ unsigned pk2(float lo, float hi) { const f32x2_pk v = {lo, hi}; return __builtin_bit_cast(unsigned, __builtin_convertvector(v, bf16x2)); }
; __device__ __forceinline__ float bf_lo(unsigned u) { return __uint_as_float(u << 16); }
; __device__ __forceinline__ float bf_hi(unsigned u) { return __uint_as_float(u & 0xffff0000u); }
; __device__ __forceinline__ void phase_pool(Frame& F, const bf16_t* XC, const bf16_t* PWT, const float* pool_scale, bf16_t* AO) {
;     ...
;         for (int kk = 0; kk < 8; ++kk) {
;             const int c0 = g * 128 + kk * 16 + hi * 8;
;             const u32x4 self = *(const u32x4*)(XC + (size_t)t * 512 + c0);
;             float s[8] = {0.f, 0.f, 0.f, 0.f, 0.f, 0.f, 0.f, 0.f};
;             for (int i = 0; i < cnt; ++i) { const u32x4 x = *(const u32x4*)(XC + (size_t)(t - i) * 512 + c0);
;                 s[0] += bf_lo(x.x); s[1] += bf_hi(x.x); s[2] += bf_lo(x.y); s[3] += bf_hi(x.y); s[4] += bf_lo(x.z); s[5] += bf_hi(x.z); s[6] += bf_lo(x.w); s[7] += bf_hi(x.w); }
;             u32x4 pa; pa.x = pk2(s[0] * rc - bf_lo(self.x), s[1] * rc - bf_hi(self.x)); pa.y = pk2(s[2] * rc - bf_lo(self.y), s[3] * rc - bf_hi(self.y));
;             pa.z = pk2(s[4] * rc - bf_lo(self.z), s[5] * rc - bf_hi(self.z)); pa.w = pk2(s[6] * rc - bf_lo(self.w), s[7] * rc - bf_hi(self.w));
;             const bf16x8 af = __builtin_bit_cast(bf16x8, pa);
; #pragma unroll
;             for (int nb = 0; nb < 4; ++nb) { const bf16x8 bfr = *(const bf16x8*)(PWT + ((size_t)g * 128 + nb * 32 + r32) * 128 + kk * 16 + hi * 8);
;                 acc[nb] = __builtin_amdgcn_mfma_f32_32x32x16_bf16(af, bfr, acc[nb], 0, 0, 0); }
;         }
.LBB0_1344:
	s_lshl_b32 s0, s21, 4
	v_lshl_add_u64 v[156:157], s[0:1], 1, v[80:81]
	v_add_co_u32_e32 v158, vcc, s15, v156
	s_nop 1
	v_addc_co_u32_e32 v159, vcc, 0, v157, vcc
	v_add_co_u32_e32 v160, vcc, s16, v156
	s_nop 1
	v_addc_co_u32_e32 v161, vcc, 0, v157, vcc
	v_add_co_u32_e32 v162, vcc, s17, v156
	s_nop 1
	v_addc_co_u32_e32 v163, vcc, 0, v157, vcc
	global_load_dwordx4 v[164:167], v[156:157], off
	global_load_dwordx4 v[168:171], v[158:159], off
	global_load_dwordx4 v[172:175], v[160:161], off
	global_load_dwordx4 v[176:179], v[162:163], off
	v_lshl_add_u32 v155, s0, 1, v149
	s_nop 0
	s_nop 0
	ds_read_b128 v[64:67], v155
	v_mov_b32_e32 v84, 0
	s_mov_b64 s[4:5], 0
	v_mov_b32_e32 v92, v155
	v_mov_b32_e32 v77, v72
	v_mov_b32_e32 v85, v84
	v_mov_b32_e32 v86, v84
	v_mov_b32_e32 v87, v84
	v_mov_b32_e32 v88, v84
	v_mov_b32_e32 v89, v84
	v_mov_b32_e32 v90, v84
	v_mov_b32_e32 v91, v84
.LBB0_1345:
	ds_read_b128 v[98:101], v92
	v_add_co_u32_e32 v77, vcc, 1, v77
	v_add_u32_e32 v92, 0xfffffef0, v92
	s_or_b64 s[4:5], vcc, s[4:5]
	s_waitcnt lgkmcnt(0)
	v_lshlrev_b32_e32 v102, 16, v98
	v_and_b32_e32 v103, 0xffff0000, v98
	v_lshlrev_b32_e32 v98, 16, v99
	v_and_b32_e32 v99, 0xffff0000, v99
	v_lshlrev_b32_e32 v104, 16, v100
	v_and_b32_e32 v105, 0xffff0000, v100
	v_lshlrev_b32_e32 v100, 16, v101
	v_and_b32_e32 v101, 0xffff0000, v101
	v_pk_add_f32 v[90:91], v[90:91], v[102:103]
	v_pk_add_f32 v[88:89], v[88:89], v[98:99]
	v_pk_add_f32 v[86:87], v[86:87], v[104:105]
	v_pk_add_f32 v[84:85], v[84:85], v[100:101]
	s_andn2_b64 exec, exec, s[4:5]
	s_cbranch_execnz .LBB0_1345
	s_or_b64 exec, exec, s[4:5]
	v_lshlrev_b32_e32 v108, 16, v66
	v_and_b32_e32 v109, 0xffff0000, v66
	v_lshlrev_b32_e32 v66, 16, v67
	v_and_b32_e32 v67, 0xffff0000, v67
	v_pk_fma_f32 v[84:85], v[74:75], v[84:85], v[66:67] neg_lo:[0,0,1] neg_hi:[0,0,1]
	v_lshlrev_b32_e32 v106, 16, v64
	v_and_b32_e32 v107, 0xffff0000, v64
	v_lshlrev_b32_e32 v64, 16, v65
	v_and_b32_e32 v65, 0xffff0000, v65
	v_cvt_pk_bf16_f32 v67, v84, v85
	v_pk_fma_f32 v[88:89], v[74:75], v[88:89], v[64:65] neg_lo:[0,0,1] neg_hi:[0,0,1]
	s_nop 0
	v_cvt_pk_bf16_f32 v65, v88, v89
	v_pk_fma_f32 v[90:91], v[74:75], v[90:91], v[106:107] neg_lo:[0,0,1] neg_hi:[0,0,1]
	v_pk_fma_f32 v[86:87], v[74:75], v[86:87], v[108:109] neg_lo:[0,0,1] neg_hi:[0,0,1]
	v_cvt_pk_bf16_f32 v64, v90, v91
	v_cvt_pk_bf16_f32 v66, v86, v87
	s_add_i32 s21, s21, 1
	s_cmp_eq_u32 s21, 8
	v_lshl_add_u64 v[82:83], v[82:83], 0, 32
	s_waitcnt vmcnt(3)
	v_mfma_f32_32x32x16_bf16 v[48:63], v[164:167], v[64:67], v[48:63]
	s_waitcnt vmcnt(2)
	v_mfma_f32_32x32x16_bf16 v[32:47], v[168:171], v[64:67], v[32:47]
	s_waitcnt vmcnt(1)
	v_mfma_f32_32x32x16_bf16 v[16:31], v[172:175], v[64:67], v[16:31]
	s_waitcnt vmcnt(0)
	v_mfma_f32_32x32x16_bf16 v[0:15], v[176:179], v[64:67], v[0:15]
	s_cbranch_scc0 .LBB0_1344
; __device__ __forceinline__ unsigned f2bf(float f) { unsigned u = __builtin_bit_cast(unsigned, f); return (u + 0x7fffu + ((u >> 16) & 1u)) >> 16; }
; __device__ __forceinline__ void phase_pool(Frame& F, const bf16_t* XC, const bf16_t* PWT, const float* pool_scale, bf16_t* AO) {
;     ...
; #pragma unroll
;         for (int nb = 0; nb < 4; ++nb) { const int col = g * 128 + nb * 32 + r32; const float sc = pool_scale[col];
; #pragma unroll
;             for (int r = 0; r < 16; ++r) { const int row = (r & 3) + 8 * (r >> 2) + 4 * hi; AO[(size_t)(t0 + row) * DM + col] = (bf16_t)f2bf(acc[nb][r] * sc); } }
	v_readlane_b32 s36, v237, 27
	v_readlane_b32 s37, v237, 28
	v_readlane_b32 s4, v237, 45
	v_readlane_b32 s5, v237, 46
	v_add_u32_e32 v66, s20, v69
	v_add_u32_e32 v64, s19, v94
	v_lshlrev_b32_e32 v74, 1, v66
	v_lshlrev_b32_e32 v66, 2, v66
	v_ashrrev_i32_e32 v65, 31, v64
	v_mov_b32_e32 v75, 0
	v_lshlrev_b64 v[64:65], 11, v[64:65]
	global_load_dwordx4 v[100:103], v66, s[36:37]
	global_load_dwordx4 v[104:107], v66, s[36:37] offset:32
	global_load_dwordx4 v[108:111], v66, s[36:37] offset:64
	global_load_dwordx4 v[112:115], v66, s[36:37] offset:96
	global_load_dwordx4 v[116:119], v66, s[36:37] offset:128
	global_load_dwordx4 v[120:123], v66, s[36:37] offset:160
	global_load_dwordx4 v[124:127], v66, s[36:37] offset:192
	global_load_dwordx4 v[128:131], v66, s[36:37] offset:224
	global_load_dwordx4 v[132:135], v66, s[36:37] offset:256
	global_load_dwordx4 v[136:139], v66, s[36:37] offset:288
	global_load_dwordx4 v[140:143], v66, s[36:37] offset:320
	global_load_dwordx4 v[144:147], v66, s[36:37] offset:352
	global_load_dwordx4 v[148:151], v66, s[36:37] offset:384
	global_load_dwordx4 v[152:155], v66, s[36:37] offset:416
	global_load_dwordx4 v[156:159], v66, s[36:37] offset:448
	global_load_dwordx4 v[160:163], v66, s[36:37] offset:480
	v_lshl_add_u64 v[64:65], s[4:5], 0, v[64:65]
	v_lshl_add_u64 v[64:65], v[64:65], 0, v[74:75]
	v_readlane_b32 s38, v237, 29
	v_readlane_b32 s39, v237, 30
	v_readlane_b32 s40, v237, 31
	v_readlane_b32 s41, v237, 32
	v_readlane_b32 s42, v237, 33
	v_readlane_b32 s43, v237, 34
	v_readlane_b32 s44, v237, 35
	v_readlane_b32 s45, v237, 36
	v_readlane_b32 s46, v237, 37
	v_readlane_b32 s47, v237, 38
	v_readlane_b32 s48, v237, 39
	v_readlane_b32 s49, v237, 40
	v_readlane_b32 s50, v237, 41
	v_readlane_b32 s51, v237, 42
	s_waitcnt vmcnt(12)
	v_pk_mul_f32 v[48:49], v[48:49], v[100:101]
	v_pk_mul_f32 v[50:51], v[50:51], v[102:103]
	v_cvt_pk_bf16_f32 v48, v48, v49
	v_cvt_pk_bf16_f32 v49, v50, v51
	global_store_dwordx2 v[64:65], v[48:49], off
	v_pk_mul_f32 v[52:53], v[52:53], v[104:105]
	v_pk_mul_f32 v[54:55], v[54:55], v[106:107]
	v_cvt_pk_bf16_f32 v52, v52, v53
	v_cvt_pk_bf16_f32 v53, v54, v55
	global_store_dwordx2 v[64:65], v[52:53], off offset:16
	v_pk_mul_f32 v[56:57], v[56:57], v[108:109]
	v_pk_mul_f32 v[58:59], v[58:59], v[110:111]
	v_cvt_pk_bf16_f32 v56, v56, v57
	v_cvt_pk_bf16_f32 v57, v58, v59
	global_store_dwordx2 v[64:65], v[56:57], off offset:32
	v_pk_mul_f32 v[60:61], v[60:61], v[112:113]
	v_pk_mul_f32 v[62:63], v[62:63], v[114:115]
	v_cvt_pk_bf16_f32 v60, v60, v61
	v_cvt_pk_bf16_f32 v61, v62, v63
	global_store_dwordx2 v[64:65], v[60:61], off offset:48
	s_waitcnt vmcnt(12)
	v_pk_mul_f32 v[32:33], v[32:33], v[116:117]
	v_pk_mul_f32 v[34:35], v[34:35], v[118:119]
	v_cvt_pk_bf16_f32 v32, v32, v33
	v_cvt_pk_bf16_f32 v33, v34, v35
	global_store_dwordx2 v[64:65], v[32:33], off offset:64
	v_pk_mul_f32 v[36:37], v[36:37], v[120:121]
	v_pk_mul_f32 v[38:39], v[38:39], v[122:123]
	v_cvt_pk_bf16_f32 v36, v36, v37
	v_cvt_pk_bf16_f32 v37, v38, v39
	global_store_dwordx2 v[64:65], v[36:37], off offset:80
	v_pk_mul_f32 v[40:41], v[40:41], v[124:125]
	v_pk_mul_f32 v[42:43], v[42:43], v[126:127]
	v_cvt_pk_bf16_f32 v40, v40, v41
	v_cvt_pk_bf16_f32 v41, v42, v43
	global_store_dwordx2 v[64:65], v[40:41], off offset:96
	v_pk_mul_f32 v[44:45], v[44:45], v[128:129]
	v_pk_mul_f32 v[46:47], v[46:47], v[130:131]
	v_cvt_pk_bf16_f32 v44, v44, v45
	v_cvt_pk_bf16_f32 v45, v46, v47
	global_store_dwordx2 v[64:65], v[44:45], off offset:112
	s_waitcnt vmcnt(12)
	v_pk_mul_f32 v[16:17], v[16:17], v[132:133]
	v_pk_mul_f32 v[18:19], v[18:19], v[134:135]
	v_cvt_pk_bf16_f32 v16, v16, v17
	v_cvt_pk_bf16_f32 v17, v18, v19
	global_store_dwordx2 v[64:65], v[16:17], off offset:128
	v_pk_mul_f32 v[20:21], v[20:21], v[136:137]
	v_pk_mul_f32 v[22:23], v[22:23], v[138:139]
	v_cvt_pk_bf16_f32 v20, v20, v21
	v_cvt_pk_bf16_f32 v21, v22, v23
	global_store_dwordx2 v[64:65], v[20:21], off offset:144
	v_pk_mul_f32 v[24:25], v[24:25], v[140:141]
	v_pk_mul_f32 v[26:27], v[26:27], v[142:143]
	v_cvt_pk_bf16_f32 v24, v24, v25
	v_cvt_pk_bf16_f32 v25, v26, v27
	global_store_dwordx2 v[64:65], v[24:25], off offset:160
	v_pk_mul_f32 v[28:29], v[28:29], v[144:145]
	v_pk_mul_f32 v[30:31], v[30:31], v[146:147]
	v_cvt_pk_bf16_f32 v28, v28, v29
	v_cvt_pk_bf16_f32 v29, v30, v31
	global_store_dwordx2 v[64:65], v[28:29], off offset:176
	s_waitcnt vmcnt(12)
	v_pk_mul_f32 v[0:1], v[0:1], v[148:149]
	v_pk_mul_f32 v[2:3], v[2:3], v[150:151]
	v_cvt_pk_bf16_f32 v0, v0, v1
	v_cvt_pk_bf16_f32 v1, v2, v3
	global_store_dwordx2 v[64:65], v[0:1], off offset:192
	v_pk_mul_f32 v[4:5], v[4:5], v[152:153]
	v_pk_mul_f32 v[6:7], v[6:7], v[154:155]
	v_cvt_pk_bf16_f32 v4, v4, v5
	v_cvt_pk_bf16_f32 v5, v6, v7
	global_store_dwordx2 v[64:65], v[4:5], off offset:208
	v_pk_mul_f32 v[8:9], v[8:9], v[156:157]
	v_pk_mul_f32 v[10:11], v[10:11], v[158:159]
	v_cvt_pk_bf16_f32 v8, v8, v9
	v_cvt_pk_bf16_f32 v9, v10, v11
	global_store_dwordx2 v[64:65], v[8:9], off offset:224
	v_pk_mul_f32 v[12:13], v[12:13], v[160:161]
	v_pk_mul_f32 v[14:15], v[14:15], v[162:163]
	v_cvt_pk_bf16_f32 v12, v12, v13
	v_cvt_pk_bf16_f32 v13, v14, v15
	global_store_dwordx2 v[64:65], v[12:13], off offset:240
	s_add_i32 s6, s6, s7
	s_cmpk_gt_i32 s6, 0xfff
	s_cbranch_scc0 .LBB0_1343
